# v63 + rider memory block diet: context-unit checks replaced by a negative tile counter at unit start, the four LDS staging writes paired into two ds_write2_b32
# baseline (speedup 1.0000x reference)
; DI void attn_unit_d8(unsigned char* lds, const AttnArgs& a) {
;     ...
;     f32x16 o0[2], o1[2];
; #pragma unroll
;     for (int d = 0; d < 2; ++d) { o0[d] = (f32x16){}; o1[d] = (f32x16){}; }
;     f32x4 l0 = {0.f, 0.f, 0.f, 0.f}, l1 = {0.f, 0.f, 0.f, 0.f};
;     ...
;     int sb = 0;
;     const v8i zz8 = (v8i){0, 0, 0, 0, 0, 0, 0, 0};
;     v8i PaX = zz8, PbX = zz8, PaY = zz8, PbY = zz8, vX0 = zz8, vX1 = zz8, vY0 = zz8, vY1 = zz8;
.LBB0_662:
	s_and_b32 s61, s42, 1
	s_lshl_b32 s61, s61, 3
	s_sub_i32 s61, 0, s61
	s_cmpk_gt_i32 s42, 0x1ff
	s_cselect_b32 s61, -64, s61
	v_mov_b32_e32 v2, 0
	s_mov_b32 s16, 0
	v_mov_b32_e32 v138, 0
	v_mov_b32_e32 v139, 0
	v_mov_b32_e32 v140, 0
	v_mov_b32_e32 v141, 0
	v_mov_b32_e32 v142, 0
	v_mov_b32_e32 v143, 0
	v_mov_b32_e32 v144, 0
	v_mov_b32_e32 v145, 0
	v_mov_b32_e32 v130, 0
	v_mov_b32_e32 v131, 0
	v_mov_b32_e32 v132, 0
	v_mov_b32_e32 v133, 0
	v_mov_b32_e32 v134, 0
	v_mov_b32_e32 v135, 0
	v_mov_b32_e32 v136, 0
	v_mov_b32_e32 v137, 0
	v_mov_b32_e32 v154, 0
	v_mov_b32_e32 v155, 0
	v_mov_b32_e32 v156, 0
	v_mov_b32_e32 v157, 0
	v_mov_b32_e32 v158, 0
	v_mov_b32_e32 v159, 0
	v_mov_b32_e32 v160, 0
	v_mov_b32_e32 v161, 0
	v_mov_b32_e32 v146, 0
	v_mov_b32_e32 v147, 0
	v_mov_b32_e32 v148, 0
	v_mov_b32_e32 v149, 0
	v_mov_b32_e32 v150, 0
	v_mov_b32_e32 v151, 0
	v_mov_b32_e32 v152, 0
	v_mov_b32_e32 v153, 0
	v_mov_b32_e32 v3, v2
	v_mov_b32_e32 v4, v2
	v_mov_b32_e32 v5, v2
	v_mov_b32_e32 v6, v2
	v_mov_b32_e32 v7, v2
	v_mov_b32_e32 v8, v2
	v_mov_b32_e32 v9, v2
	v_mov_b32_e32 v10, v2
	v_mov_b32_e32 v11, v2
	v_mov_b32_e32 v12, v2
	v_mov_b32_e32 v13, v2
	v_mov_b32_e32 v14, v2
	v_mov_b32_e32 v15, v2
	v_mov_b32_e32 v16, v2
	v_mov_b32_e32 v17, v2
	v_mov_b32_e32 v18, v2
	v_mov_b32_e32 v19, v2
	v_mov_b32_e32 v20, v2
	v_mov_b32_e32 v21, v2
	v_mov_b32_e32 v22, v2
	v_mov_b32_e32 v23, v2
	v_mov_b32_e32 v24, v2
	v_mov_b32_e32 v25, v2
	v_mov_b32_e32 v26, v2
	v_mov_b32_e32 v27, v2
	v_mov_b32_e32 v28, v2
	v_mov_b32_e32 v29, v2
	v_mov_b32_e32 v30, v2
	v_mov_b32_e32 v31, v2
	v_mov_b32_e32 v32, v2
	v_mov_b32_e32 v33, v2
	v_mov_b32_e32 v50, v2
	v_mov_b32_e32 v51, v2
	v_mov_b32_e32 v52, v2
	v_mov_b32_e32 v53, v2
	v_mov_b32_e32 v54, v2
	v_mov_b32_e32 v55, v2
	v_mov_b32_e32 v56, v2
	v_mov_b32_e32 v57, v2
	v_mov_b32_e32 v58, v2
	v_mov_b32_e32 v59, v2
	v_mov_b32_e32 v60, v2
	v_mov_b32_e32 v61, v2
	v_mov_b32_e32 v62, v2
	v_mov_b32_e32 v63, v2
	v_mov_b32_e32 v64, v2
	v_mov_b32_e32 v65, v2
	v_mov_b32_e32 v34, v2
	v_mov_b32_e32 v35, v2
	v_mov_b32_e32 v36, v2
	v_mov_b32_e32 v37, v2
	v_mov_b32_e32 v38, v2
	v_mov_b32_e32 v39, v2
	v_mov_b32_e32 v40, v2
	v_mov_b32_e32 v41, v2
	v_mov_b32_e32 v42, v2
	v_mov_b32_e32 v43, v2
	v_mov_b32_e32 v44, v2
	v_mov_b32_e32 v45, v2
	v_mov_b32_e32 v46, v2
	v_mov_b32_e32 v47, v2
	v_mov_b32_e32 v48, v2
	v_mov_b32_e32 v49, v2
	v_mov_b32_e32 v186, v2
	v_mov_b32_e32 v187, v2
	v_mov_b32_e32 v184, v2
	v_mov_b32_e32 v185, v2
	v_mov_b32_e32 v190, v2
	v_mov_b32_e32 v191, v2
	v_mov_b32_e32 v188, v2
	v_mov_b32_e32 v189, v2

; DI unsigned pk4_fp8_mul64(float a, float b, float c, float d) { v2s_t r = {0, 0}; r = __builtin_amdgcn_cvt_scalef32_pk_fp8_f32(r, a, b, 0.015625f, false); r = __builtin_amdgcn_cvt_scalef32_pk_fp8_f32(r, c, d, 0.015625f, true); return __builtin_bit_cast(unsigned, r); }
; DI void attn_unit_a8(unsigned char* lds, const AttnArgs& a) {
;     ...
;     auto w_cvt = [&]() __attribute__((always_inline)) { unsigned char* t8 = lds + AT_WT + wn4 * WPITCH + 4 * wid;
; #pragma unroll
;         for (int j = 0; j < 4; ++j) *(unsigned*)(t8 + j * WPITCH) = pk4_fp8_mul64(wq[0][j], wq[1][j], wq[2][j], wq[3][j]); };
;     const int wcol = tid >> 1, whalf = tid & 1;
;     const unsigned wper_gu = (unsigned)((wcol >> 7) * 256 + (wcol & 96) + invperm32(wcol & 31)) * 1024u + 16u * whalf;
;     const unsigned wper_dn = (unsigned)fwd_lane16(wcol) * 1024u + 16u * whalf;
;     auto w_store = [&](int j) __attribute__((always_inline)) { const float* src; unsigned char* dst; int ld, n0, k0; bool gu; w_decode(j, src, dst, ld, n0, k0, gu);
;         const int nb = n0 >> 8; const unsigned uni = (unsigned)(gu ? (nb & 3) * 512 + (nb >> 2) * 128 : nb * 256) * 1024u + (unsigned)k0;
;         const unsigned off = (gu ? wper_gu : wper_dn) + uni;
;         const unsigned* t = (const unsigned*)(lds + AT_WT + wcol * WPITCH + 16 * whalf);
;         *(u32x4*)(dst + off) = (u32x4){t[0], t[1], t[2], t[3]}; };
.Lmy_rd0_nodec:
	s_add_i32 s72, s61, -1
	s_cmp_lt_u32 s72, 24
	s_cbranch_scc0 .Lmy_rd0_noc
	s_waitcnt vmcnt(4)
	v_cvt_scalef32_pk_fp8_f32 v236, v236, v240, s62
	v_cvt_scalef32_pk_fp8_f32 v237, v237, v241, s62
	v_cvt_scalef32_pk_fp8_f32 v238, v238, v242, s62
	v_cvt_scalef32_pk_fp8_f32 v239, v239, v243, s62
	v_cvt_scalef32_pk_fp8_f32 v236, v244, v248, s62 op_sel:[0,0,0,1]
	v_cvt_scalef32_pk_fp8_f32 v237, v245, v249, s62 op_sel:[0,0,0,1]
	v_cvt_scalef32_pk_fp8_f32 v238, v246, v250, s62 op_sel:[0,0,0,1]
	v_cvt_scalef32_pk_fp8_f32 v239, v247, v251, s62 op_sel:[0,0,0,1]
	ds_write2_b32 v252, v236, v237 offset1:9
	ds_write2_b32 v252, v238, v239 offset0:18 offset1:27
.Lmy_rd0_noc:
	ds_read2_b32 v[244:245], v253 offset1:1
	ds_read2_b32 v[246:247], v253 offset0:2 offset1:3
	s_add_i32 s72, s61, -2
	s_cmp_lt_u32 s72, 24
	s_cbranch_scc0 .Lmy_rd0_sdum
	s_andn2_b32 s73, s65, 1
	s_add_u32 s82, s70, s73
	s_addc_u32 s83, s71, 0
	s_bitcmp1_b32 s65, 0
	s_cbranch_scc1 .Lmy_rd0_sdn
	s_waitcnt lgkmcnt(0)
	global_store_dwordx4 v254, v[244:247], s[82:83]
	s_branch .Lmy_rd0_sdone

; DI void attn_unit_a8(unsigned char* lds, const AttnArgs& a) {
;     ...
;     auto w_issue = [&](int j) __attribute__((always_inline)) { const float* src; unsigned char* dst; int ld, n0, k0; bool gu; w_decode(j, src, dst, ld, n0, k0, gu);
;         const float* p = src + (size_t)(k0 + 4 * wid) * ld + n0 + wn4;
;         wq[0] = __builtin_nontemporal_load((const f32x4*)p); wq[1] = __builtin_nontemporal_load((const f32x4*)(p + ld));
;         wq[2] = __builtin_nontemporal_load((const f32x4*)(p + (size_t)2 * ld)); wq[3] = __builtin_nontemporal_load((const f32x4*)(p + (size_t)3 * ld)); };
.Lmy_rd0_sdone:
	s_cmp_lt_u32 s61, 24
	s_cbranch_scc1 .Lmy_rd0_lgo
	s_mov_b64 s[84:85], s[70:71]
	s_mov_b32 s80, 0

; DI void attn_unit_d8(unsigned char* lds, const AttnArgs& a) {
;     ...
;     f32x16 o0[2], o1[2];
; #pragma unroll
;     for (int d = 0; d < 2; ++d) { o0[d] = (f32x16){}; o1[d] = (f32x16){}; }
;     f32x4 l0 = {0.f, 0.f, 0.f, 0.f}, l1 = {0.f, 0.f, 0.f, 0.f};
;     ...
;     int sb = 0;
;     const v8i zz8 = (v8i){0, 0, 0, 0, 0, 0, 0, 0};
;     v8i PaX = zz8, PbX = zz8, PaY = zz8, PbY = zz8, vX0 = zz8, vX1 = zz8, vY0 = zz8, vY1 = zz8;
.LBB0_1887:
	s_and_b32 s61, s46, 1
	s_lshl_b32 s61, s61, 3
	s_sub_i32 s61, 0, s61
	s_cmpk_gt_i32 s46, 0x1ff
	s_cselect_b32 s61, -64, s61
	s_ashr_i32 s21, s20, 31
	s_lshl_b64 s[20:21], s[20:21], 8
	s_add_u32 s8, s24, s20
	s_addc_u32 s20, s25, s21
	s_add_u32 s8, s8, s47
	s_addc_u32 s21, s20, 0
	s_add_u32 s20, s8, 0x800000
	v_mov_b32_e32 v2, 0
	s_addc_u32 s21, s21, 0
	s_mov_b32 s23, 0
	s_mov_b32 s22, -2
	v_mov_b32_e32 v138, 0
	v_mov_b32_e32 v139, 0
	v_mov_b32_e32 v140, 0
	v_mov_b32_e32 v141, 0
	v_mov_b32_e32 v142, 0
	v_mov_b32_e32 v143, 0
	v_mov_b32_e32 v144, 0
	v_mov_b32_e32 v145, 0
	v_mov_b32_e32 v130, 0
	v_mov_b32_e32 v131, 0
	v_mov_b32_e32 v132, 0
	v_mov_b32_e32 v133, 0
	v_mov_b32_e32 v134, 0
	v_mov_b32_e32 v135, 0
	v_mov_b32_e32 v136, 0
	v_mov_b32_e32 v137, 0
	v_mov_b32_e32 v154, 0
	v_mov_b32_e32 v155, 0
	v_mov_b32_e32 v156, 0
	v_mov_b32_e32 v157, 0
	v_mov_b32_e32 v158, 0
	v_mov_b32_e32 v159, 0
	v_mov_b32_e32 v160, 0
	v_mov_b32_e32 v161, 0
	v_mov_b32_e32 v146, 0
	v_mov_b32_e32 v147, 0
	v_mov_b32_e32 v148, 0
	v_mov_b32_e32 v149, 0
	v_mov_b32_e32 v150, 0
	v_mov_b32_e32 v151, 0
	v_mov_b32_e32 v152, 0
	v_mov_b32_e32 v153, 0
	v_mov_b32_e32 v3, v2
	v_mov_b32_e32 v4, v2
	v_mov_b32_e32 v5, v2
	v_mov_b32_e32 v6, v2
	v_mov_b32_e32 v7, v2
	v_mov_b32_e32 v8, v2
	v_mov_b32_e32 v9, v2
	v_mov_b32_e32 v10, v2
	v_mov_b32_e32 v11, v2
	v_mov_b32_e32 v12, v2
	v_mov_b32_e32 v13, v2
	v_mov_b32_e32 v14, v2
	v_mov_b32_e32 v15, v2
	v_mov_b32_e32 v16, v2
	v_mov_b32_e32 v17, v2
	v_mov_b32_e32 v18, v2
	v_mov_b32_e32 v19, v2
	v_mov_b32_e32 v20, v2
	v_mov_b32_e32 v21, v2
	v_mov_b32_e32 v22, v2
	v_mov_b32_e32 v23, v2
	v_mov_b32_e32 v24, v2
	v_mov_b32_e32 v25, v2
	v_mov_b32_e32 v26, v2
	v_mov_b32_e32 v27, v2
	v_mov_b32_e32 v28, v2
	v_mov_b32_e32 v29, v2
	v_mov_b32_e32 v30, v2
	v_mov_b32_e32 v31, v2
	v_mov_b32_e32 v32, v2
	v_mov_b32_e32 v33, v2
	v_mov_b32_e32 v50, v2
	v_mov_b32_e32 v51, v2
	v_mov_b32_e32 v52, v2
	v_mov_b32_e32 v53, v2
	v_mov_b32_e32 v54, v2
	v_mov_b32_e32 v55, v2
	v_mov_b32_e32 v56, v2
	v_mov_b32_e32 v57, v2
	v_mov_b32_e32 v58, v2
	v_mov_b32_e32 v59, v2
	v_mov_b32_e32 v60, v2
	v_mov_b32_e32 v61, v2
	v_mov_b32_e32 v62, v2
	v_mov_b32_e32 v63, v2
	v_mov_b32_e32 v64, v2
	v_mov_b32_e32 v65, v2
	v_mov_b32_e32 v34, v2
	v_mov_b32_e32 v35, v2
	v_mov_b32_e32 v36, v2
	v_mov_b32_e32 v37, v2
	v_mov_b32_e32 v38, v2
	v_mov_b32_e32 v39, v2
	v_mov_b32_e32 v40, v2
	v_mov_b32_e32 v41, v2
	v_mov_b32_e32 v42, v2
	v_mov_b32_e32 v43, v2
	v_mov_b32_e32 v44, v2
	v_mov_b32_e32 v45, v2
	v_mov_b32_e32 v46, v2
	v_mov_b32_e32 v47, v2
	v_mov_b32_e32 v48, v2
	v_mov_b32_e32 v49, v2
	v_mov_b32_e32 v188, v2
	v_mov_b32_e32 v189, v2
	v_mov_b32_e32 v186, v2
	v_mov_b32_e32 v187, v2
	v_mov_b32_e32 v192, v2
	v_mov_b32_e32 v193, v2
	v_mov_b32_e32 v190, v2
	v_mov_b32_e32 v191, v2
